# mixer queue: Q-blocks 15..4 whole, 3..0 split in halves
# baseline (speedup 1.0000x reference)
.LBB0_476:
	v_readlane_b32 s0, v254, 24
	s_waitcnt lgkmcnt(0)
	s_barrier
	v_mov_b32_e32 v0, s0
	ds_read_b32 v0, v0
	s_waitcnt lgkmcnt(0)
	v_readfirstlane_b32 s48, v0
	s_cmp_eq_u32 s48, -1
	s_cbranch_scc1 .LBB0_509
	s_lshr_b32 s19, s48, 8
	s_and_b32 s57, s48, 0xff
	s_cmpk_lt_u32 s57, 0x58
	s_mov_b64 s[0:1], -1
	s_cbranch_scc0 .LBB0_846
	s_and_b32 s0, s48, 0xfc
	s_cmp_lg_u32 s0, 4
	s_mov_b64 s[0:1], -1
	s_cbranch_scc0 .LBB0_830
	s_cmp_gt_u32 s57, 3
	s_cbranch_scc0 .LBB0_797
	s_cmp_gt_u32 s57, 55
	s_cbranch_scc0 .LBB0_767
	s_cmp_gt_u32 s57, 79
	s_cbranch_scc1 .Lhalves_keep
	s_bitcmp1_b32 s57, 0
	s_cbranch_scc1 .LBB0_458
	s_sub_i32 s0, s57, 56
	s_lshr_b32 s0, s0, 1
	s_sub_i32 s30, 15, s0
	s_branch .Lwhole_entry
